# Fourier stage B output: workgroup-level LDS transposition (one extra barrier per unit) so every store instruction writes full 256 B row segments (K and V) instead of per-wave 64 B pieces; plus previou
# speedup vs baseline: 1.0018x; 1.0018x over previous
; #define LAS __attribute__((address_space(3)))
;     __device__ __forceinline__ bf16_t* dft() const { return (bf16_t*)(ws + WS_DFT); }
;     __device__ __forceinline__ bf16_t* dn() const { return (bf16_t*)(ws + WS_DN); }
;     __device__ __forceinline__ bf16_t* proj() const { return (bf16_t*)(ws + WS_PROJ); }
; __device__ __forceinline__ int v_st(int k, int c) { const int kk = (k & ~0xC) | ((k & 4) << 1) | ((k & 8) >> 1); return ((kk >> 3) * 4 + (c >> 5)) * 512 + ((kk & 7) * 32 + (c & 31)) * 2; }
; __device__ __forceinline__ int v_rd_base(int lane) { return ((lane & 3) << 3) | (((lane >> 2) & 3) << 6) | (((lane >> 4) & 1) << 5) | (((lane >> 5) & 1) << 8); }
; __device__ __forceinline__ void phase_fft_b(const Frame& F) {
;     const int tid = F.tid, wid = F.wid, lane = F.lane, r32 = lane & 31, hi = lane >> 5;
;     LAS char* Vt = (LAS char*)F.lds;
;     const int sr = tid >> 4, sc = (tid & 15) * 8;
;     const int rb = wid & 1, cq = wid >> 1, k2 = 32 * rb + r32;
;     const bf16_t* dc = F.dft() + 32768; const bf16_t* ds = dc + 4096; const bf16_t* dn = dc + 8192;
;     bf16x8 bc[4], bs[4], bn[4];
; #pragma unroll
;     for (int ks = 0; ks < 4; ++ks) { const int o = k2 * 64 + ks * 16 + hi * 8; bc[ks] = *(const bf16x8*)(dc + o); bs[ks] = *(const bf16x8*)(ds + o); bn[ks] = *(const bf16x8*)(dn + o); }
;     const int NU = NB * 128 * 4;
;     bf16x8 pf[4];
;     ...
;     int u = F.wg, par = 0;
;     if (u < NU) FB_LOAD(u);
;     for (; u < NU; u += F.nwg, par ^= 1) {
;         const int b = u >> 9, k1 = (u >> 2) & 127, cb = u & 3;
;         LAS char* img = Vt + par * 32768;
; #pragma unroll
;         for (int q = 0; q < 4; ++q) *(LAS bf16x8*)(img + (q >> 1) * 16384 + ff::v_st((q & 1) * 32 + sr, sc)) = pf[q];
;         __syncthreads();
;         if (u + F.nwg < NU) FB_LOAD(u + F.nwg);
;         f32x16 ar = f32x16{}, bi = f32x16{};
;         const int vbP = (int)(uintptr_t)img + ff::v_rd_base(lane) + cq * 512;
;         ff::xt_two<0>(ar, bi, vbP, bc, bs);
;         ff::xt_two<0>(ar, bi, vbP + 16384, bn, bc);
;         bf16_t* op = F.proj() + (size_t)(b * SEQ + k1 + 128 * k2) * INW + cb * 128 + 32 * cq + 4 * hi;
.LBB0_508:
	s_andn2_b64 vcc, exec, s[8:9]
	s_cbranch_vccnz .LBB0_585
	v_readlane_b32 s8, v252, 42
	s_waitcnt vmcnt(0)
	v_mov_b32_e32 v2, v0
	v_readlane_b32 s9, v252, 43
	s_andn2_b64 vcc, exec, s[8:9]
	v_readfirstlane_b32 s0, v2
	v_mov_b32_e32 v136, 0xffff8000
	v_mov_b32_e32 v137, 0xffffa000
	v_mov_b32_e32 v138, 0xffffc000
	v_mov_b32_e32 v139, 0xa000
	v_mov_b32_e32 v140, 0xc000
	v_mov_b32_e32 v141, 0x10000
	v_mov_b32_e32 v142, 0x12000
	v_mov_b32_e32 v143, 0x14000
	v_mov_b32_e32 v144, 0x16000
	v_mov_b32_e32 v145, 0x18000
	v_mov_b32_e32 v148, 0x1a000
	v_mov_b32_e32 v149, 0x1c000
	s_cbranch_vccnz .LBB0_516
	s_lshr_b32 s1, s0, 1
	s_add_u32 s8, s56, 0xd0000
	v_and_b32_e32 v1, 31, v2
	s_addc_u32 s9, s57, 0
	v_and_or_b32 v1, s1, 32, v1
	s_add_u32 s18, s56, 0xd2000
	v_bfe_u32 v3, v2, 5, 1
	s_addc_u32 s19, s57, 0
	v_lshlrev_b32_e32 v1, 7, v1
	s_add_u32 s22, s56, 0xd4000
	v_lshl_or_b32 v4, v3, 4, v1
	v_ashrrev_i32_e32 v100, 4, v2
	v_readlane_b32 s1, v253, 1
	s_addc_u32 s23, s57, 0
	v_or_b32_e32 v5, 32, v4
	v_add_u32_e32 v6, s1, v100
	global_load_dwordx4 v[34:37], v4, s[8:9]
	global_load_dwordx4 v[38:41], v4, s[18:19]
	global_load_dwordx4 v[42:45], v4, s[22:23]
	global_load_dwordx4 v[46:49], v5, s[8:9]
	global_load_dwordx4 v[50:53], v5, s[18:19]
	global_load_dwordx4 v[54:57], v5, s[22:23]
	v_or_b32_e32 v5, 64, v4
	s_ashr_i32 s0, s0, 7
	v_ashrrev_i32_e32 v7, 31, v6
	global_load_dwordx4 v[58:61], v5, s[8:9]
	global_load_dwordx4 v[62:65], v5, s[18:19]
	v_or_b32_e32 v4, 0x60, v4
	global_load_dwordx4 v[66:69], v5, s[22:23]
	global_load_dwordx4 v[70:73], v4, s[8:9]
	global_load_dwordx4 v[74:77], v4, s[18:19]
	global_load_dwordx4 v[78:81], v4, s[22:23]
	s_add_u32 s8, s56, 0x3d316100
	v_lshlrev_b64 v[8:9], 11, v[6:7]
	v_add_u32_e32 v6, 32, v6
	v_lshlrev_b32_e32 v5, 3, v2
	s_addc_u32 s9, s57, 0
	v_readlane_b32 s1, v252, 57
	v_ashrrev_i32_e32 v7, 31, v6
	v_and_b32_e32 v4, 0x78, v5
	v_lshl_add_u64 v[8:9], s[8:9], 0, v[8:9]
	s_lshl_b32 s76, s1, 1
	v_lshlrev_b64 v[6:7], 11, v[6:7]
	v_lshl_add_u64 v[8:9], v[8:9], 0, s[76:77]
	v_lshlrev_b32_e32 v146, 1, v4
	v_lshl_add_u64 v[6:7], s[8:9], 0, v[6:7]
	v_lshl_add_u64 v[8:9], v[8:9], 0, v[146:147]
	v_lshl_add_u64 v[6:7], v[6:7], 0, s[76:77]
	v_lshl_add_u64 v[6:7], v[6:7], 0, v[146:147]
	global_load_dwordx4 v[82:85], v[8:9], off
	global_load_dwordx4 v[86:89], v[8:9], off offset:1024
	global_load_dwordx4 v[90:93], v[6:7], off
	global_load_dwordx4 v[94:97], v[6:7], off offset:1024
	v_lshrrev_b32_e32 v7, 1, v100
	v_and_b32_e32 v8, 3, v100
	v_and_b32_e32 v6, 63, v2
	v_and_or_b32 v7, v7, 4, v8
	v_lshlrev_b32_e32 v101, 6, v7
	v_lshlrev_b32_e32 v7, 4, v2
	v_lshlrev_b32_e32 v6, 3, v6
	v_and_b32_e32 v102, 48, v7
	v_and_b32_e32 v8, 24, v6
	v_and_b32_e32 v7, 0xc0, v7
	v_lshlrev_b32_e32 v2, 1, v2
	s_lshl_b32 s1, s0, 9
	v_and_b32_e32 v2, 32, v2
	v_and_b32_e32 v6, 0x100, v6
	v_or3_b32 v7, v7, s1, v8
	v_or3_b32 v103, v7, v2, v6
	v_lshlrev_b32_e32 v2, 2, v3
	v_and_b32_e32 v3, 0xfffff0, v100
	v_lshlrev_b32_e32 v6, 1, v100
	v_and_or_b32 v3, v6, 8, v3
	v_bfe_u32 v5, v5, 5, 2
	v_lshrrev_b32_e32 v3, 1, v3
	v_or_b32_e32 v3, v3, v5
	v_lshlrev_b32_e32 v104, 9, v3
	v_add_u32_e32 v3, 32, v100
	v_and_b32_e32 v6, 0xfffff0, v3
	v_lshlrev_b32_e32 v3, 1, v3
	s_lshl_b32 s18, s0, 5
	v_and_or_b32 v3, v3, 8, v6
	s_ashr_i32 s19, s18, 31
	v_lshrrev_b32_e32 v3, 1, v3
	v_or_b32_e32 v3, v3, v5
	s_add_u32 s22, s56, 0x1c316100
	v_readlane_b32 s24, v254, 62
	v_lshlrev_b32_e32 v105, 9, v3
	s_addc_u32 s23, s57, 0
	s_mov_b32 s0, 0
	v_lshlrev_b32_e32 v98, 1, v4
	v_lshlrev_b32_e32 v146, 1, v2
	v_readlane_b32 s1, v254, 6
	v_readlane_b32 s30, v253, 15
	s_mov_b32 s31, s24
	v_readlane_b32 s25, v254, 63
	v_and_b32_e32 v122, 31, v0
	v_bfe_u32 v123, v0, 6, 1
	v_lshl_or_b32 v122, v123, 5, v122
	v_mul_u32_u24_e32 v122, 0x210, v122
	v_lshrrev_b32_e32 v123, 7, v0
	v_lshl_add_u32 v122, v123, 6, v122
	v_bfe_u32 v123, v0, 5, 1
	v_lshl_add_u32 v122, v123, 3, v122
	v_add_u32_e32 v122, 0x12800, v122
	v_lshrrev_b32_e32 v123, 5, v0
	v_mul_u32_u24_e32 v123, 0x210, v123
	v_and_b32_e32 v124, 31, v0
	v_lshl_add_u32 v123, v124, 4, v123
	v_add_u32_e32 v123, 0x12800, v123
	v_lshrrev_b32_e32 v1, 5, v0
	v_lshlrev_b32_e32 v1, 7, v1
	v_bfe_u32 v146, v0, 4, 1
	v_lshlrev_b32_e32 v146, 10, v146
	v_and_b32_e32 v124, 15, v0
	v_lshl_add_u32 v146, v124, 4, v146
	s_waitcnt vmcnt(0)
	s_branch .LBB0_512
; __device__ __forceinline__ unsigned cvt_pk_bf16(float lo, float hi) { unsigned r; asm volatile("v_cvt_pk_bf16_f32 %0, %1, %2" : "=v"(r) : "v"(lo), "v"(hi)); return r; }
;     __device__ __forceinline__ bf16_t* proj() const { return (bf16_t*)(ws + WS_PROJ); }
; __device__ __forceinline__ int v_rd_base(int lane) { return ((lane & 3) << 3) | (((lane >> 2) & 3) << 6) | (((lane >> 4) & 1) << 5) | (((lane >> 5) & 1) << 8); }
; __device__ __forceinline__ void phase_fft_b(const Frame& F) {
;     ...
;         f32x16 ar = f32x16{}, bi = f32x16{};
;         const int vbP = (int)(uintptr_t)img + ff::v_rd_base(lane) + cq * 512;
;         ff::xt_two<0>(ar, bi, vbP, bc, bs);
;         ff::xt_two<0>(ar, bi, vbP + 16384, bn, bc);
;         bf16_t* op = F.proj() + (size_t)(b * SEQ + k1 + 128 * k2) * INW + cb * 128 + 32 * cq + 4 * hi;
; #pragma unroll
;         for (int g = 0; g < 4; ++g) {
;             u32x2 wa, wb;
;             wa.x = cvt_pk_bf16(ar[4 * g] * 0.011048543456039806f, ar[4 * g + 1] * 0.011048543456039806f); wa.y = cvt_pk_bf16(ar[4 * g + 2] * 0.011048543456039806f, ar[4 * g + 3] * 0.011048543456039806f);
;             wb.x = cvt_pk_bf16(bi[4 * g] * 0.011048543456039806f, bi[4 * g + 1] * 0.011048543456039806f); wb.y = cvt_pk_bf16(bi[4 * g + 2] * 0.011048543456039806f, bi[4 * g + 3] * 0.011048543456039806f);
;             *(u32x2*)(op + C_K + 8 * g) = wa; *(u32x2*)(op + C_V + 8 * g) = wb;
;         }
.LBB0_511:
	v_add_u32_e32 v99, s40, v103
	ds_read_b64_tr_b16 v[2:3], v99 offset:0
	ds_read_b64_tr_b16 v[4:5], v99 offset:0x800
	ds_read_b64_tr_b16 v[106:107], v99 offset:0x1000
	ds_read_b64_tr_b16 v[108:109], v99 offset:0x1800
	ds_read_b64_tr_b16 v[110:111], v99 offset:0x2000
	ds_read_b64_tr_b16 v[112:113], v99 offset:0x2800
	ds_read_b64_tr_b16 v[114:115], v99 offset:0x3000
	ds_read_b64_tr_b16 v[116:117], v99 offset:0x3800
	s_waitcnt lgkmcnt(0)
	s_bfe_u32 s28, s31, 0x70002
	v_mfma_f32_32x32x16_bf16 v[18:33], v[2:5], v[34:37], 0
	v_add_u32_e32 v99, 0x4000, v99
	v_mfma_f32_32x32x16_bf16 v[2:17], v[2:5], v[38:41], 0
	v_mfma_f32_32x32x16_bf16 v[18:33], v[106:109], v[46:49], v[18:33]
	v_mfma_f32_32x32x16_bf16 v[2:17], v[106:109], v[50:53], v[2:17]
	ds_read_b64_tr_b16 v[106:107], v99 offset:0
	ds_read_b64_tr_b16 v[108:109], v99 offset:0x800
	v_mfma_f32_32x32x16_bf16 v[18:33], v[110:113], v[58:61], v[18:33]
	v_mfma_f32_32x32x16_bf16 v[2:17], v[110:113], v[62:65], v[2:17]
	ds_read_b64_tr_b16 v[110:111], v99 offset:0x1000
	ds_read_b64_tr_b16 v[112:113], v99 offset:0x1800
	v_mfma_f32_32x32x16_bf16 v[18:33], v[114:117], v[70:73], v[18:33]
	v_mfma_f32_32x32x16_bf16 v[2:17], v[114:117], v[74:77], v[2:17]
	ds_read_b64_tr_b16 v[114:115], v99 offset:0x2000
	ds_read_b64_tr_b16 v[116:117], v99 offset:0x2800
	ds_read_b64_tr_b16 v[118:119], v99 offset:0x3000
	ds_read_b64_tr_b16 v[120:121], v99 offset:0x3800
	s_waitcnt lgkmcnt(0)
	v_mfma_f32_32x32x16_bf16 v[18:33], v[106:109], v[42:45], v[18:33]
	s_and_b32 s29, s1, 0xffffe000
	s_or_b32 s28, s29, s28
	s_xor_b32 s0, s0, 1
	s_andn2_b64 vcc, exec, s[24:25]
	s_mov_b32 s31, s2
	v_mfma_f32_32x32x16_bf16 v[2:17], v[106:109], v[34:37], v[2:17]
	v_or_b32_e32 v106, s28, v1
	v_ashrrev_i32_e32 v107, 31, v106
	v_lshlrev_b64 v[106:107], 13, v[106:107]
	s_and_b32 s28, s30, 0x180
	v_lshl_add_u64 v[106:107], s[22:23], 0, v[106:107]
	s_lshl_b32 s76, s28, 1
	v_lshl_add_u64 v[106:107], v[106:107], 0, s[76:77]
	v_mfma_f32_32x32x16_bf16 v[18:33], v[110:113], v[54:57], v[18:33]
	v_lshl_add_u64 v[106:107], v[106:107], 0, v[146:147]
	v_readlane_b32 s28, v254, 7
	s_add_i32 s1, s1, s28
	s_mov_b32 s30, s7
	v_mfma_f32_32x32x16_bf16 v[2:17], v[110:113], v[46:49], v[2:17]
	v_mfma_f32_32x32x16_bf16 v[18:33], v[114:117], v[66:69], v[18:33]
	v_mfma_f32_32x32x16_bf16 v[2:17], v[114:117], v[58:61], v[2:17]
	v_mfma_f32_32x32x16_bf16 v[18:33], v[118:121], v[78:81], v[18:33]
	v_mfma_f32_32x32x16_bf16 v[2:17], v[118:121], v[70:73], v[2:17]
	s_nop 10
	v_mul_f32_e32 v18, 0x3c3504f3, v18
	v_mul_f32_e32 v19, 0x3c3504f3, v19
	v_mul_f32_e32 v20, 0x3c3504f3, v20
	v_mul_f32_e32 v21, 0x3c3504f3, v21
	v_cvt_pk_bf16_f32 v166, v18, v19
	v_cvt_pk_bf16_f32 v167, v20, v21
	ds_write_b64 v122, v[166:167]
	v_mul_f32_e32 v2, 0x3c3504f3, v2
	v_mul_f32_e32 v3, 0x3c3504f3, v3
	v_mul_f32_e32 v4, 0x3c3504f3, v4
	v_mul_f32_e32 v5, 0x3c3504f3, v5
	v_cvt_pk_bf16_f32 v168, v2, v3
	v_cvt_pk_bf16_f32 v169, v4, v5
	ds_write_b64 v122, v[168:169] offset:256
	v_mul_f32_e32 v22, 0x3c3504f3, v22
	v_mul_f32_e32 v23, 0x3c3504f3, v23
	v_mul_f32_e32 v24, 0x3c3504f3, v24
	v_mul_f32_e32 v25, 0x3c3504f3, v25
	v_cvt_pk_bf16_f32 v170, v22, v23
	v_cvt_pk_bf16_f32 v171, v24, v25
	ds_write_b64 v122, v[170:171] offset:16
	v_mul_f32_e32 v6, 0x3c3504f3, v6
	v_mul_f32_e32 v7, 0x3c3504f3, v7
	v_mul_f32_e32 v8, 0x3c3504f3, v8
	v_mul_f32_e32 v9, 0x3c3504f3, v9
	v_cvt_pk_bf16_f32 v172, v6, v7
	v_cvt_pk_bf16_f32 v173, v8, v9
	ds_write_b64 v122, v[172:173] offset:272
	v_mul_f32_e32 v26, 0x3c3504f3, v26
	v_mul_f32_e32 v27, 0x3c3504f3, v27
	v_mul_f32_e32 v28, 0x3c3504f3, v28
	v_mul_f32_e32 v29, 0x3c3504f3, v29
	v_cvt_pk_bf16_f32 v174, v26, v27
	v_cvt_pk_bf16_f32 v175, v28, v29
	ds_write_b64 v122, v[174:175] offset:32
	v_mul_f32_e32 v10, 0x3c3504f3, v10
	v_mul_f32_e32 v11, 0x3c3504f3, v11
	v_mul_f32_e32 v12, 0x3c3504f3, v12
	v_mul_f32_e32 v13, 0x3c3504f3, v13
	v_cvt_pk_bf16_f32 v176, v10, v11
	v_cvt_pk_bf16_f32 v177, v12, v13
	ds_write_b64 v122, v[176:177] offset:288
	v_mul_f32_e32 v30, 0x3c3504f3, v30
	v_mul_f32_e32 v31, 0x3c3504f3, v31
	v_mul_f32_e32 v32, 0x3c3504f3, v32
	v_mul_f32_e32 v33, 0x3c3504f3, v33
	v_cvt_pk_bf16_f32 v178, v30, v31
	v_cvt_pk_bf16_f32 v179, v32, v33
	ds_write_b64 v122, v[178:179] offset:48
	v_mul_f32_e32 v14, 0x3c3504f3, v14
	v_mul_f32_e32 v15, 0x3c3504f3, v15
	v_mul_f32_e32 v16, 0x3c3504f3, v16
	v_mul_f32_e32 v17, 0x3c3504f3, v17
	v_cvt_pk_bf16_f32 v180, v14, v15
	v_cvt_pk_bf16_f32 v181, v16, v17
	ds_write_b64 v122, v[180:181] offset:304
	s_waitcnt lgkmcnt(0)
	s_barrier
	ds_read_b128 v[150:153], v123
	ds_read_b128 v[154:157], v123 offset:8448
	ds_read_b128 v[158:161], v123 offset:16896
	ds_read_b128 v[162:165], v123 offset:25344
	s_mov_b64 s[28:29], 0x1000000
	v_lshl_add_u64 v[124:125], v[106:107], 0, s[28:29]
	v_lshl_add_u64 v[126:127], v[124:125], 0, s[28:29]
	v_lshl_add_u64 v[128:129], v[126:127], 0, s[28:29]
	s_waitcnt lgkmcnt(3)
	global_store_dwordx4 v[106:107], v[150:153], off offset:1024
	s_waitcnt lgkmcnt(2)
	global_store_dwordx4 v[124:125], v[154:157], off offset:1024
	s_waitcnt lgkmcnt(1)
	global_store_dwordx4 v[126:127], v[158:161], off offset:1024
	s_waitcnt lgkmcnt(0)
	global_store_dwordx4 v[128:129], v[162:165], off offset:1024
	s_cbranch_vccz .LBB0_516
